# MLA main loop: exp2 work spread evenly over all MFMA gaps (13 of the C1 exps deferred into the next tile step), on top of LDS-DMA pieces inside the QK MFMA gaps
# speedup vs baseline: 1.0062x; 1.0062x over previous
; #define WAITV(n) asm volatile("s_waitcnt vmcnt(%0)" ::"n"(n) : "memory")
; #define SBAR() do { asm volatile("s_waitcnt lgkmcnt(0)" ::: "memory"); __builtin_amdgcn_s_barrier(); asm volatile("" ::: "memory"); } while (0)
; DEV int otid() { int t = threadIdx.x; asm volatile("" : "+v"(t)); return t; }
; DEV unsigned char* ows_(unsigned char* w) { gptr_t g = (gptr_t)w; asm volatile("" : "+s"(g)); return (unsigned char*)g; }
; DEV unsigned lds_addr(LAS char* p) { return (unsigned)(uintptr_t)p; }
; #define MLA_ISSUE(t_, st_) do { const unsigned char* s_ = imgs + (size_t)(t_) * MLA_IMG + wid * (STG / 8) + lane * 16; const unsigned d_ = ldsw + (unsigned)((st_) * STG); \
;     _Pragma("unroll") for (int i_ = 0; i_ < STG / 8192; ++i_) glds16a(s_ + i_ * 1024, d_ + i_ * 1024); } while (0)
; template <int VAR> DEV void mla_unit(const Params& p, int layer, int b, int hd, int tokbase, int t0, int t1, LAS char* lds, SideJob& sj) {
;     unsigned char* ws = ows_(p.ws); const int tid = otid(), lane = tid & 63, wid = tid >> 6, r = lane & 31, h = lane >> 5;
;     constexpr int STG = MLA_IMG;
;     const float cinit = 15.0f - ((const float*)(ws + WS_SCAL))[layer * 8 + 1];
;     const int tok = tokbase + 32 * wid + r;
;     v8i qf[2];
; #pragma unroll
;     for (int sx = 0; sx < 2; ++sx) { const u32x4* q8 = (const u32x4*)(ws + WS_QC + (size_t)tok * 768 + hd * 128 + 64 * sx + 32 * h); const u32x4 a = q8[0], bq = q8[1];
;         qf[sx] = (v8i){(int)a[0], (int)a[1], (int)a[2], (int)a[3], (int)bq[0], (int)bq[1], (int)bq[2], (int)bq[3]}; }
;     const unsigned char* imgs = ws + WS_KVC + (size_t)((b * 6 + hd) * 130) * MLA_IMG;
;     const unsigned ldsw = (unsigned)__builtin_amdgcn_readfirstlane((int)(lds_addr(lds) + (unsigned)(wid * (STG / 8))));
;     ...
;     f32x16 cini, sA0, sA1, sB0, sB1, o0, o1, lacc;
; #pragma unroll
;     for (int i = 0; i < 16; ++i) { cini[i] = cinit; o0[i] = 0.f; o1[i] = 0.f; lacc[i] = 0.f; }
;     const unsigned koffl = (unsigned)(2 * h * 1024 + r * 16);
;     const unsigned voffl = (unsigned)MLA_VOFF + (unsigned)(2 * h * 1024 + r * 16);
;     const int ns = t1 - t0;
;     MLA_ISSUE(t0, 0);
;     WAITV(0); SBAR();
.LBB0_808:
	s_and_b64 vcc, exec, s[6:7]
	s_cbranch_vccz .LBB0_749
	s_ashr_i32 s2, s64, 6
	s_mul_hi_i32 s3, s2, 0x2aaaaaab
	s_lshr_b32 s6, s3, 31
	s_add_i32 s3, s3, s6
	s_mul_i32 s6, s3, 6
	s_sub_i32 s37, s2, s6
	s_lshl_b32 s6, s64, 8
	s_lshl_b32 s3, s3, 14
	s_and_b32 s6, s6, 0x3f00
	s_or_b32 s3, s3, s6
	s_mov_b64 s[6:7], s[38:39]
	v_mov_b32_e32 v52, v246
	s_lshl_b64 s[8:9], s[48:49], 2
	v_and_b32_e32 v7, 31, v52
	v_ashrrev_i32_e32 v6, 6, v52
	s_add_u32 s8, s6, s8
	v_or_b32_e32 v2, s3, v7
	s_addc_u32 s9, s7, s9
	v_lshl_add_u32 v180, v6, 5, v2
	v_mov_b64_e32 v[2:3], s[6:7]
	s_movk_i32 s3, 0x300
	global_load_dword v8, v247, s[8:9] offset:4
	v_mad_i64_i32 v[2:3], s[8:9], v180, s3, v[2:3]
	s_lshl_b32 s8, s37, 7
	s_ashr_i32 s9, s8, 31
	v_lshl_add_u64 v[2:3], v[2:3], 0, s[8:9]
	v_and_b32_e32 v178, 32, v52
	v_lshl_add_u64 v[2:3], v[2:3], 0, v[178:179]
	s_mov_b64 s[8:9], 0x33370100
	s_mov_b32 s3, 0x33370000
	v_lshl_add_u64 v[4:5], v[2:3], 0, s[8:9]
	v_add_co_u32_e32 v2, vcc, s3, v2
	s_mul_i32 s3, s2, 0x82
	s_nop 0
	v_addc_co_u32_e32 v3, vcc, 0, v3, vcc
	global_load_dwordx4 v[138:141], v[2:3], off offset:256
	global_load_dwordx4 v[142:145], v[4:5], off offset:16
	global_load_dwordx4 v[134:137], v[4:5], off offset:80
	global_load_dwordx4 v[130:133], v[4:5], off offset:64
	s_mul_i32 s8, s2, 0x30c000
	s_movk_i32 s2, 0xc00
	s_mul_hi_i32 s9, s3, 0x6000
	v_mul_lo_u32 v50, v6, s2
	s_add_u32 s20, s6, s8
	v_and_b32_e32 v3, 63, v52
	v_bfe_u32 v198, v52, 5, 1
	s_addc_u32 s21, s7, s9
	v_lshlrev_b32_e32 v4, 4, v7
	v_ashrrev_i32_e32 v51, 31, v50
	v_lshl_or_b32 v199, v198, 11, v4
	v_lshl_add_u64 v[4:5], s[20:21], 0, v[50:51]
	v_lshlrev_b32_e32 v178, 4, v3
	v_readfirstlane_b32 s60, v50
	v_lshl_add_u64 v[18:19], v[4:5], 0, v[178:179]
	s_mov_b64 s[20:21], 0x35800100
	s_add_i32 s60, s60, 0
	v_lshl_add_u64 v[4:5], v[18:19], 0, s[20:21]
	s_mov_b32 s2, m0
	s_mov_b32 m0, s60
	s_nop 0
	global_load_lds_dwordx4 v[4:5], off
	s_mov_b32 m0, s2
	s_mov_b64 s[20:21], 0x35800500
	v_lshl_add_u64 v[4:5], v[18:19], 0, s[20:21]
	s_add_i32 s2, s60, 0x400
	s_mov_b32 s3, m0
	s_mov_b32 m0, s2
	s_nop 0
	global_load_lds_dwordx4 v[4:5], off
	s_mov_b32 m0, s3
	s_mov_b64 s[20:21], 0x35800900
	v_lshl_add_u64 v[4:5], v[18:19], 0, s[20:21]
	s_add_i32 s2, s60, 0x800
	s_mov_b32 s3, m0
	s_mov_b32 m0, s2
	s_nop 0
	global_load_lds_dwordx4 v[4:5], off
	s_mov_b32 m0, s3
	s_waitcnt vmcnt(0)
	s_waitcnt lgkmcnt(0)
	s_barrier
; #define LAS __attribute__((address_space(3)))
; #define WAITV(n) asm volatile("s_waitcnt vmcnt(%0)" ::"n"(n) : "memory")
; #define SBAR() do { asm volatile("s_waitcnt lgkmcnt(0)" ::: "memory"); __builtin_amdgcn_s_barrier(); asm volatile("" ::: "memory"); } while (0)
; DEV float ex2(float x) { return __builtin_amdgcn_exp2f(x); }
; #define MFMA8(a, b, c) __builtin_amdgcn_mfma_scale_f32_32x32x64_f8f6f4((a), (b), (c), 0, 0, 0, 0x7f7f7f7f, 0, 0x7c7c7c7c)
; #define MLA_ISSUE(t_, st_) do { const unsigned char* s_ = imgs + (size_t)(t_) * MLA_IMG + wid * (STG / 8) + lane * 16; const unsigned d_ = ldsw + (unsigned)((st_) * STG); \
;     _Pragma("unroll") for (int i_ = 0; i_ < STG / 8192; ++i_) glds16a(s_ + i_ * 1024, d_ + i_ * 1024); } while (0)
; template <int VAR> DEV void mla_unit(const Params& p, int layer, int b, int hd, int tokbase, int t0, int t1, LAS char* lds, SideJob& sj) {
;     ...
;     f32x16 cini, sA0, sA1, sB0, sB1, o0, o1, lacc;
; #pragma unroll
;     for (int i = 0; i < 16; ++i) { cini[i] = cinit; o0[i] = 0.f; o1[i] = 0.f; lacc[i] = 0.f; }
;     const unsigned koffl = (unsigned)(2 * h * 1024 + r * 16);
;     const unsigned voffl = (unsigned)MLA_VOFF + (unsigned)(2 * h * 1024 + r * 16);
;     const int ns = t1 - t0;
;     MLA_ISSUE(t0, 0);
;     WAITV(0); SBAR();
;     if (ns > 1) MLA_ISSUE(t0 + 1, 1);
;     { LAS char* kp = lds + koffl;
;       sA0 = MFMA8(mla_kf8(kp, 0, 0), qf[0], cini); sA1 = MFMA8(mla_kf8(kp, 1, 0), qf[0], cini);
;       sA0 = MFMA8(mla_kf8(kp, 0, 1), qf[1], sA0); sA1 = MFMA8(mla_kf8(kp, 1, 1), qf[1], sA1);
; #pragma unroll
;       for (int i = 0; i < 16; ++i) { sA0[i] = ex2(sA0[i]); sA1[i] = ex2(sA1[i]); } }
;     int slot = 0;
;     v8i pw = {0, 0, 0, 0, 0, 0, 0, 0};
	s_mov_b64 s[20:21], 0x35806100
	v_lshl_add_u64 v[20:21], v[18:19], 0, s[20:21]
	s_add_i32 s2, s60, 0x6000
	s_mov_b32 s3, m0
	s_mov_b32 m0, s2
	s_nop 0
	global_load_lds_dwordx4 v[20:21], off
	s_mov_b32 m0, s3
	s_mov_b64 s[20:21], 0x35806500
	v_lshl_add_u64 v[20:21], v[18:19], 0, s[20:21]
	s_add_i32 s2, s60, 0x6400
	s_mov_b32 s3, m0
	s_mov_b32 m0, s2
	s_nop 0
	global_load_lds_dwordx4 v[20:21], off
	s_mov_b32 m0, s3
	s_mov_b64 s[20:21], 0x35806900
	v_lshl_add_u64 v[18:19], v[18:19], 0, s[20:21]
	s_add_i32 s2, s60, 0x6800
	s_mov_b32 s3, m0
	s_mov_b32 m0, s2
	s_nop 0
	global_load_lds_dwordx4 v[18:19], off
	s_mov_b32 m0, s3
	v_add_u32_e32 v200, 0, v199
	ds_read_b128 v[18:21], v200
	ds_read_b128 v[22:25], v200 offset:1024
	s_waitcnt vmcnt(0)
	v_ashrrev_i32_e32 v191, 4, v52
	s_movk_i32 s2, 0x104
	v_ashrrev_i32_e32 v195, 3, v52
	v_ashrrev_i32_e32 v181, 31, v180
	s_mov_b32 s62, 0
	v_mov_b32_e32 v193, v179
	v_mov_b32_e32 v146, 0
	v_mov_b32_e32 v147, 0
	v_mov_b32_e32 v148, 0
	v_mov_b32_e32 v149, 0
	v_mov_b32_e32 v150, 0
	v_mov_b32_e32 v151, 0
	v_mov_b32_e32 v152, 0
	v_mov_b32_e32 v153, 0
	s_mov_b32 s61, 0
	v_sub_f32_e32 v2, 0x41700000, v8
	v_mov_b32_e32 v3, v2
	v_mov_b32_e32 v4, v2
	v_mov_b32_e32 v5, v2
	v_mov_b32_e32 v6, v2
	v_mov_b32_e32 v7, v2
	v_mov_b32_e32 v8, v2
	v_mov_b32_e32 v9, v2
	v_mov_b32_e32 v10, v2
	v_mov_b32_e32 v11, v2
	v_mov_b32_e32 v12, v2
	v_mov_b32_e32 v13, v2
	v_mov_b32_e32 v14, v2
	v_mov_b32_e32 v15, v2
	v_mov_b32_e32 v16, v2
	v_mov_b32_e32 v17, v2
	s_waitcnt lgkmcnt(0)
	s_nop 0
	v_mfma_scale_f32_32x32x64_f8f6f4 v[18:33], v[18:25], v[138:145], v[2:17], v209, v208 op_sel_hi:[0,0,0]
	ds_read_b128 v[34:37], v200 offset:512
	ds_read_b128 v[38:41], v200 offset:1536
	s_waitcnt lgkmcnt(0)
	v_mfma_scale_f32_32x32x64_f8f6f4 v[34:49], v[34:41], v[138:145], v[2:17], v209, v208 op_sel_hi:[0,0,0]
	ds_read_b128 v[54:57], v200 offset:4096
	ds_read_b128 v[58:61], v200 offset:5120
	s_waitcnt lgkmcnt(0)
	v_mfma_scale_f32_32x32x64_f8f6f4 v[18:33], v[54:61], v[130:137], v[18:33], v209, v208 op_sel_hi:[0,0,0]
	ds_read_b128 v[54:57], v200 offset:4608
	ds_read_b128 v[58:61], v200 offset:5632
	s_waitcnt lgkmcnt(0)
	v_mfma_scale_f32_32x32x64_f8f6f4 v[34:49], v[54:61], v[130:137], v[34:49], v209, v208 op_sel_hi:[0,0,0]
	s_nop 15
	v_exp_f32_e32 v82, v18
	v_lshlrev_b32_e32 v18, 2, v52
	v_and_b32_e32 v190, 60, v18
	v_exp_f32_e32 v83, v19
	v_mul_lo_u32 v18, v191, s2
	s_add_i32 s2, 0, 0x12000
	v_lshlrev_b32_e32 v19, 2, v190
	v_add3_u32 v194, s2, v18, v19
	v_lshlrev_b32_e32 v18, 3, v52
	v_exp_f32_e32 v84, v20
	v_exp_f32_e32 v85, v21
	v_exp_f32_e32 v86, v22
	v_exp_f32_e32 v87, v23
	v_exp_f32_e32 v88, v24
	v_exp_f32_e32 v89, v25
	v_exp_f32_e32 v66, v34
	v_exp_f32_e32 v67, v35
	v_exp_f32_e32 v68, v36
	v_mov_b32_e32 v69, v37
	v_mov_b32_e32 v70, v38
	v_mov_b32_e32 v71, v39
	v_mov_b32_e32 v72, v40
	v_mov_b32_e32 v73, v41
	v_mov_b32_e32 v74, v42
	v_mov_b32_e32 v75, v43
	v_mov_b32_e32 v76, v44
	v_mov_b32_e32 v77, v45
	v_mov_b32_e32 v78, v46
	v_mov_b32_e32 v79, v47
	v_mov_b32_e32 v80, v48
	v_mov_b32_e32 v81, v49
	v_exp_f32_e32 v90, v26
	v_exp_f32_e32 v91, v27
	v_exp_f32_e32 v92, v28
	v_exp_f32_e32 v93, v29
	v_exp_f32_e32 v94, v30
	v_exp_f32_e32 v95, v31
	v_exp_f32_e32 v96, v32
	v_exp_f32_e32 v97, v33
	v_and_b32_e32 v192, 56, v18
	v_or_b32_e32 v18, s8, v178
	v_mov_b32_e32 v19, s9
	v_lshl_add_u64 v[18:19], v[18:19], 0, v[50:51]
	v_lshl_add_u64 v[18:19], s[6:7], 0, v[18:19]
	s_mov_b64 s[8:9], 0x3580c100
	v_mov_b32_e32 v34, 0
	v_cmp_lt_u32_e64 s[40:41], 31, v190
	v_lshl_add_u32 v196, v195, 2, s2
	v_mul_u32_u24_e32 v197, 0x104, v192
	v_lshl_add_u64 v[162:163], v[18:19], 0, s[8:9]
	v_mov_b32_e32 v35, v34
	v_mov_b32_e32 v36, v34
	v_mov_b32_e32 v37, v34
	v_mov_b32_e32 v38, v34
	v_mov_b32_e32 v39, v34
	v_mov_b32_e32 v40, v34
	v_mov_b32_e32 v41, v34
	v_mov_b32_e32 v42, v34
	v_mov_b32_e32 v43, v34
	v_mov_b32_e32 v44, v34
	v_mov_b32_e32 v45, v34
	v_mov_b32_e32 v46, v34
	v_mov_b32_e32 v47, v34
	v_mov_b32_e32 v48, v34
	v_mov_b32_e32 v49, v34
	v_mov_b32_e32 v18, v34
	v_mov_b32_e32 v19, v34
	v_mov_b32_e32 v20, v34
	v_mov_b32_e32 v21, v34
	v_mov_b32_e32 v22, v34
	v_mov_b32_e32 v23, v34
	v_mov_b32_e32 v24, v34
	v_mov_b32_e32 v25, v34
	v_mov_b32_e32 v26, v34
	v_mov_b32_e32 v27, v34
	v_mov_b32_e32 v28, v34
	v_mov_b32_e32 v29, v34
	v_mov_b32_e32 v30, v34
	v_mov_b32_e32 v31, v34
	v_mov_b32_e32 v32, v34
	v_mov_b32_e32 v33, v34
	v_mov_b32_e32 v50, v34
	v_mov_b32_e32 v51, v34
	v_mov_b32_e32 v52, v34
	v_mov_b32_e32 v53, v34
	v_mov_b32_e32 v54, v34
	v_mov_b32_e32 v55, v34
	v_mov_b32_e32 v56, v34
	v_mov_b32_e32 v57, v34
	v_mov_b32_e32 v58, v34
	v_mov_b32_e32 v59, v34
	v_mov_b32_e32 v60, v34
	v_mov_b32_e32 v61, v34
	v_mov_b32_e32 v62, v34
	v_mov_b32_e32 v63, v34
	v_mov_b32_e32 v64, v34
	v_mov_b32_e32 v65, v34
	s_branch .LBB0_813

; #define LAS __attribute__((address_space(3)))
; #define WAITV(n) asm volatile("s_waitcnt vmcnt(%0)" ::"n"(n) : "memory")
; template <int VAR> DEV void mla_step(f32x16& C0, f32x16& C1, f32x16& P0, f32x16& P1, f32x16& o0, f32x16& o1, f32x16& lacc,
;                   const v8i (&qf)[2], const f32x16& cini, LAS char* kp, LAS char* vp, v8i& pw) {
;     v8i kf[2], vf[2];
;     const v8i ones8 = {0x38383838, 0x38383838, 0x38383838, 0x38383838, 0x38383838, 0x38383838, 0x38383838, 0x38383838};
;     kf[0] = mla_kf8(kp, 0, 0); kf[1] = mla_kf8(kp, 1, 0);
;     MLA_SB();
; #pragma unroll
;     for (int g = 0; g < 4; ++g) {
;         const int kb = g & 1, sx = g >> 1;
;         if (kb) C1 = MFMA8(kf[1], qf[sx], sx == 0 ? cini : C1); else C0 = MFMA8(kf[0], qf[sx], sx == 0 ? cini : C0);
;         if (g < 2) kf[kb] = mla_kf8(kp, kb, 1);
;         if (g >= 2) vf[g - 2] = mla_vf8(vp, g - 2);
; #pragma unroll
;         for (int j = 0; j < 2; ++j) { const int w = 2 * g + j, e = 4 * w;
;             if (VAR == 3) pw[w] = __builtin_bit_cast(int, (e < 16) ? P0[e] : P1[e - 16]);
;             else pw[w] = (int)((e < 16) ? pk_bf8x4(P0[e], P0[e + 1], P0[e + 2], P0[e + 3], pw[w]) : pk_bf8x4(P1[e - 16], P1[e - 15], P1[e - 14], P1[e - 13], pw[w])); }
;         if (g == 3) MLA_PIN(pw);
;         MLA_SB();
;     }
; #pragma unroll
;     for (int g = 0; g < 3; ++g) {
;         if (g == 0) o0 = MFMA8PV(vf[0], pw, o0); else if (g == 1) o1 = MFMA8PV(vf[1], pw, o1); else lacc = MFMA8PV(ones8, pw, lacc);
;         const int e0 = (g * 32) / 3, e1 = ((g + 1) * 32) / 3;
; #pragma unroll
;         for (int e = e0; e < e1; ++e) { if (VAR == 2 || VAR == 3) continue; if (e < 16) C0[e] = ex2(C0[e]); else C1[e - 16] = ex2(C1[e - 16]); }
;         if (g < 2) MLA_PIN(C0);
;         if (g > 0) MLA_PIN(C1);
;         MLA_SB();
;     }
; }
; template <int VAR> DEV void mla_unit(const Params& p, int layer, int b, int hd, int tokbase, int t0, int t1, LAS char* lds, SideJob& sj) {
;     ...
;     for (int s = 0; s < ns; ++s) {
;         sj_tick(p, layer, sj, lds, tid);
;         { LAS char* base = lds + slot * STG; mla_step<VAR>(sB0, sB1, sA0, sA1, o0, o1, lacc, qf, cini, base + MLA_KSUB + koffl, base + voffl, pw); }
;         if (s + 1 < ns) {
;             const int nslot = (slot == 2) ? 0 : slot + 1;
;             WAITV(0); SBAR();
;             if (s + 2 < ns) MLA_ISSUE(t0 + s + 2, (nslot == 2) ? 0 : nslot + 1);
.LBB0_812:
	s_mul_i32 s2, s62, 0x6000
	v_add_u32_e32 v172, s2, v200
	ds_read_b128 v[98:101], v172 offset:8192
	ds_read_b128 v[106:109], v172 offset:8704
	ds_read_b128 v[102:105], v172 offset:9216
	ds_read_b128 v[110:113], v172 offset:9728
	v_cvt_pk_bf8_f32 v146, v82, v83
	v_cvt_pk_bf8_f32 v147, v86, v87
	v_exp_f32_e32 v69, v69
	v_exp_f32_e32 v70, v70
	v_exp_f32_e32 v71, v71
	s_waitcnt lgkmcnt(1)
	v_mfma_scale_f32_32x32x64_f8f6f4 v[114:129], v[98:105], v[138:145], v[2:17], v209, v208 op_sel_hi:[0,0,0]
	ds_read_b128 v[154:157], v172 offset:12288
	ds_read_b128 v[158:161], v172 offset:13312
	v_cvt_pk_bf8_f32 v146, v84, v85 op_sel:[0,0,1]
	v_cvt_pk_bf8_f32 v147, v88, v89 op_sel:[0,0,1]
	v_cvt_pk_bf8_f32 v148, v90, v91
	v_cvt_pk_bf8_f32 v149, v94, v95
	ds_read_b128 v[82:85], v172 offset:12800
	ds_read_b128 v[86:89], v172 offset:13824
	v_exp_f32_e32 v72, v72
	v_exp_f32_e32 v73, v73
	s_waitcnt lgkmcnt(4)
	v_mfma_scale_f32_32x32x64_f8f6f4 v[98:113], v[106:113], v[138:145], v[2:17], v209, v208 op_sel_hi:[0,0,0]
	v_cvt_pk_bf8_f32 v148, v92, v93 op_sel:[0,0,1]
	v_cvt_pk_bf8_f32 v149, v96, v97 op_sel:[0,0,1]
	ds_read_b128 v[90:93], v172 offset:16384
	ds_read_b128 v[94:97], v172 offset:17408
	v_exp_f32_e32 v74, v74
	v_exp_f32_e32 v75, v75
	v_exp_f32_e32 v76, v76
	s_waitcnt lgkmcnt(4)
	v_mfma_scale_f32_32x32x64_f8f6f4 v[114:129], v[154:161], v[130:137], v[114:129], v209, v208 op_sel_hi:[0,0,0]
	v_exp_f32_e32 v77, v77
	v_exp_f32_e32 v78, v78
	v_exp_f32_e32 v79, v79
	v_exp_f32_e32 v80, v80
	v_exp_f32_e32 v81, v81
	s_waitcnt lgkmcnt(2)
	v_mfma_scale_f32_32x32x64_f8f6f4 v[98:113], v[82:89], v[130:137], v[98:113], v209, v208 op_sel_hi:[0,0,0]
	v_cvt_pk_bf8_f32 v150, v66, v67
	v_cvt_pk_bf8_f32 v151, v70, v71
	v_cvt_pk_bf8_f32 v150, v68, v69 op_sel:[0,0,1]
	v_cvt_pk_bf8_f32 v151, v72, v73 op_sel:[0,0,1]
	v_cvt_pk_bf8_f32 v152, v74, v75
	v_cvt_pk_bf8_f32 v153, v78, v79
	v_cvt_pk_bf8_f32 v152, v76, v77 op_sel:[0,0,1]
	v_cvt_pk_bf8_f32 v153, v80, v81 op_sel:[0,0,1]
	ds_read_b128 v[66:69], v172 offset:16896
	ds_read_b128 v[70:73], v172 offset:17920
	s_waitcnt lgkmcnt(2)
	v_mfma_scale_f32_32x32x64_f8f6f4 v[50:65], v[90:97], v[146:153], v[50:65], v209, v209 op_sel_hi:[0,0,0] blgp:1
	s_nop 0
	v_exp_f32_e32 v114, v114
	v_exp_f32_e32 v115, v115
	v_exp_f32_e32 v116, v116
	v_exp_f32_e32 v117, v117
	v_exp_f32_e32 v118, v118
	v_exp_f32_e32 v119, v119
	s_waitcnt lgkmcnt(0)
	v_mfma_scale_f32_32x32x64_f8f6f4 v[18:33], v[66:73], v[146:153], v[18:33], v209, v209 op_sel_hi:[0,0,0] blgp:1
	v_mov_b64_e32 v[160:161], s[82:83]
	v_mov_b64_e32 v[158:159], s[80:81]
	v_mov_b64_e32 v[156:157], s[78:79]
	v_mov_b64_e32 v[154:155], s[76:77]
	v_exp_f32_e32 v120, v120
	v_exp_f32_e32 v121, v121
	v_exp_f32_e32 v122, v122
	v_exp_f32_e32 v123, v123
	v_exp_f32_e32 v124, v124
	v_exp_f32_e32 v125, v125
	v_mfma_scale_f32_32x32x64_f8f6f4 v[34:49], v[154:161], v[146:153], v[34:49], v209, v209 op_sel_hi:[0,0,0] blgp:1
	v_exp_f32_e32 v126, v126
	v_exp_f32_e32 v127, v127
	v_exp_f32_e32 v128, v128
	v_exp_f32_e32 v129, v129
	v_exp_f32_e32 v98, v98
	v_exp_f32_e32 v99, v99
	v_exp_f32_e32 v100, v100
	s_add_i32 s61, s61, 1
	s_add_i32 s2, s62, 1
	s_cmp_lg_u32 s62, 2
	s_cselect_b32 s62, s2, 0
	s_mul_i32 s64, s62, 0x6000
	s_add_i32 s2, s64, 0x6000
	s_cmp_eq_u32 s62, 2
	s_cselect_b64 s[8:9], -1, 0
	s_waitcnt vmcnt(0)
	s_and_b64 s[20:21], s[8:9], exec
	s_waitcnt lgkmcnt(0)
	s_barrier
	s_cselect_b32 s2, 0, s2
	s_add_i32 s2, s2, s60
	s_mov_b32 s3, m0
	s_mov_b32 m0, s2
	v_add_u32_e32 v173, s64, v200
	ds_read_b128 v[66:69], v173
	ds_read_b128 v[74:77], v173 offset:512
	ds_read_b128 v[70:73], v173 offset:1024
	ds_read_b128 v[78:81], v173 offset:1536
	v_cvt_pk_bf8_f32 v146, v114, v115
	v_cvt_pk_bf8_f32 v147, v118, v119
	v_exp_f32_e32 v101, v101
	v_exp_f32_e32 v102, v102
	v_exp_f32_e32 v103, v103
	s_waitcnt lgkmcnt(1)
	v_mfma_scale_f32_32x32x64_f8f6f4 v[82:97], v[66:73], v[138:145], v[2:17], v209, v208 op_sel_hi:[0,0,0]
	global_load_lds_dwordx4 v[162:163], off
	ds_read_b128 v[164:167], v173 offset:4096
	ds_read_b128 v[168:171], v173 offset:5120
	v_cvt_pk_bf8_f32 v146, v116, v117 op_sel:[0,0,1]
	v_cvt_pk_bf8_f32 v147, v120, v121 op_sel:[0,0,1]
	v_cvt_pk_bf8_f32 v148, v122, v123
	v_cvt_pk_bf8_f32 v149, v126, v127
	ds_read_b128 v[114:117], v173 offset:4608
	ds_read_b128 v[118:121], v173 offset:5632
	v_exp_f32_e32 v104, v104
	v_exp_f32_e32 v105, v105
	s_waitcnt lgkmcnt(4)
	v_mfma_scale_f32_32x32x64_f8f6f4 v[66:81], v[74:81], v[138:145], v[2:17], v209, v208 op_sel_hi:[0,0,0]
	global_load_lds_dwordx4 v[162:163], off offset:1024
	v_cvt_pk_bf8_f32 v148, v124, v125 op_sel:[0,0,1]
	v_cvt_pk_bf8_f32 v149, v128, v129 op_sel:[0,0,1]
	ds_read_b128 v[122:125], v172 offset:20480
	ds_read_b128 v[126:129], v172 offset:21504
	v_exp_f32_e32 v106, v106
	v_exp_f32_e32 v107, v107
	v_exp_f32_e32 v108, v108
	s_waitcnt lgkmcnt(4)
	v_mfma_scale_f32_32x32x64_f8f6f4 v[82:97], v[164:171], v[130:137], v[82:97], v209, v208 op_sel_hi:[0,0,0]
	global_load_lds_dwordx4 v[162:163], off offset:2048
	s_mov_b32 m0, s3
	v_exp_f32_e32 v109, v109
	v_exp_f32_e32 v110, v110
	v_exp_f32_e32 v111, v111
	v_exp_f32_e32 v112, v112
	v_exp_f32_e32 v113, v113
	s_waitcnt lgkmcnt(2)
	v_mfma_scale_f32_32x32x64_f8f6f4 v[66:81], v[114:121], v[130:137], v[66:81], v209, v208 op_sel_hi:[0,0,0]
	v_cvt_pk_bf8_f32 v150, v98, v99
	v_cvt_pk_bf8_f32 v151, v102, v103
	v_cvt_pk_bf8_f32 v150, v100, v101 op_sel:[0,0,1]
	v_cvt_pk_bf8_f32 v151, v104, v105 op_sel:[0,0,1]
	v_cvt_pk_bf8_f32 v152, v106, v107
	v_cvt_pk_bf8_f32 v153, v110, v111
	v_cvt_pk_bf8_f32 v152, v108, v109 op_sel:[0,0,1]
	v_cvt_pk_bf8_f32 v153, v112, v113 op_sel:[0,0,1]
	ds_read_b128 v[98:101], v172 offset:20992
	ds_read_b128 v[102:105], v172 offset:22016
	s_waitcnt lgkmcnt(2)
	v_mfma_scale_f32_32x32x64_f8f6f4 v[50:65], v[122:129], v[146:153], v[50:65], v209, v209 op_sel_hi:[0,0,0] blgp:1
	s_nop 0
	v_exp_f32_e32 v82, v82
	v_exp_f32_e32 v83, v83
	v_exp_f32_e32 v84, v84
	v_exp_f32_e32 v85, v85
	v_exp_f32_e32 v86, v86
	v_exp_f32_e32 v87, v87
	s_waitcnt lgkmcnt(0)
	v_mfma_scale_f32_32x32x64_f8f6f4 v[18:33], v[98:105], v[146:153], v[18:33], v209, v209 op_sel_hi:[0,0,0] blgp:1
	v_exp_f32_e32 v88, v88
	v_exp_f32_e32 v89, v89
	v_exp_f32_e32 v90, v90
	v_exp_f32_e32 v91, v91
	v_exp_f32_e32 v92, v92
	v_exp_f32_e32 v93, v93
	v_mfma_scale_f32_32x32x64_f8f6f4 v[34:49], v[154:161], v[146:153], v[34:49], v209, v209 op_sel_hi:[0,0,0] blgp:1
	v_exp_f32_e32 v94, v94
	v_exp_f32_e32 v95, v95
	v_exp_f32_e32 v96, v96
	v_exp_f32_e32 v97, v97
	v_exp_f32_e32 v66, v66
	v_exp_f32_e32 v67, v67
	v_exp_f32_e32 v68, v68
	s_mov_b64 s[20:21], 0x6000
	s_cmpk_lg_i32 s61, 0x80
	v_lshl_add_u64 v[162:163], v[162:163], 0, s[20:21]
	s_cbranch_scc0 .LBB0_835

; #define LAS __attribute__((address_space(3)))
; #define WAITV(n) asm volatile("s_waitcnt vmcnt(%0)" ::"n"(n) : "memory")
; #define SBAR() do { asm volatile("s_waitcnt lgkmcnt(0)" ::: "memory"); __builtin_amdgcn_s_barrier(); asm volatile("" ::: "memory"); } while (0)
; DEV unsigned pk_bf8x4(float a, float b, float c, float d, int old = 0) { int w = __builtin_amdgcn_cvt_pk_bf8_f32(a, b, old, false); w = __builtin_amdgcn_cvt_pk_bf8_f32(c, d, w, true); return (unsigned)w; }
; #define MLA_ISSUE(t_, st_) do { const unsigned char* s_ = imgs + (size_t)(t_) * MLA_IMG + wid * (STG / 8) + lane * 16; const unsigned d_ = ldsw + (unsigned)((st_) * STG); \
;     _Pragma("unroll") for (int i_ = 0; i_ < STG / 8192; ++i_) glds16a(s_ + i_ * 1024, d_ + i_ * 1024); } while (0)
; DEV void sj_tick(const Params& p, int layer, SideJob& sj, LAS char* lds, int tid) {
;     LAS float* tile = (LAS float*)(lds + SJ_TILE_OFF);
;     const int ph = sj.g & 3; ++sj.g;
;     if (sj.le >= 64 || ph == 3) return;
;     const SjDesc d = sj_desc(p, layer, sj.le, sj.j);
; template <int VAR> DEV void mla_unit(const Params& p, int layer, int b, int hd, int tokbase, int t0, int t1, LAS char* lds, SideJob& sj) {
;     ...
;     for (int s = 0; s < ns; ++s) {
;         sj_tick(p, layer, sj, lds, tid);
;         { LAS char* base = lds + slot * STG; mla_step<VAR>(sB0, sB1, sA0, sA1, o0, o1, lacc, qf, cini, base + MLA_KSUB + koffl, base + voffl, pw); }
;         if (s + 1 < ns) {
;             const int nslot = (slot == 2) ? 0 : slot + 1;
;             WAITV(0); SBAR();
;             if (s + 2 < ns) MLA_ISSUE(t0 + s + 2, (nslot == 2) ? 0 : nslot + 1);
;             { LAS char* nb = lds + nslot * STG; LAS char* ob = lds + slot * STG; mla_step<VAR>(sA0, sA1, sB0, sB1, o0, o1, lacc, qf, cini, nb + koffl, ob + MLA_VSUB + voffl, pw); }
;             slot = nslot;
;         }
;     }
;     {
; #pragma unroll
;       for (int w = 0; w < 8; ++w) { const int e = 4 * w; pw[w] = (int)((e < 16) ? pk_bf8x4(sB0[e], sB0[e + 1], sB0[e + 2], sB0[e + 3]) : pk_bf8x4(sB1[e - 16], sB1[e - 15], sB1[e - 14], sB1[e - 13])); }
.LBB0_835:
	v_exp_f32_e32 v69, v69
	v_exp_f32_e32 v70, v70
	v_exp_f32_e32 v71, v71
	v_exp_f32_e32 v72, v72
	v_exp_f32_e32 v73, v73
	v_exp_f32_e32 v74, v74
	v_exp_f32_e32 v75, v75
	v_exp_f32_e32 v76, v76
	v_exp_f32_e32 v77, v77
	v_exp_f32_e32 v78, v78
	v_exp_f32_e32 v79, v79
	v_exp_f32_e32 v80, v80
	v_exp_f32_e32 v81, v81
	s_add_i32 s2, s29, s61
	s_and_b32 s66, s2, 3
	s_cmp_gt_i32 s33, 63
	s_cselect_b64 s[20:21], -1, 0
	s_cmp_eq_u32 s66, 3
	s_cselect_b64 s[50:51], -1, 0
	s_or_b64 s[20:21], s[20:21], s[50:51]
	s_and_b64 vcc, exec, s[20:21]
	s_cbranch_vccnz .LBB0_858
	s_add_i32 s50, s33, s12
	s_cmpk_lt_i32 s36, 0x100
	s_cselect_b64 s[52:53], -1, 0
	s_lshl_b32 s60, s36, 6
	s_cmpk_gt_i32 s36, 0xff
	s_mov_b64 s[58:59], -1
	s_cbranch_scc1 .LBB0_838
	s_ashr_i32 s51, s50, 31
	s_lshl_b64 s[54:55], s[50:51], 21
	s_add_u32 s20, s44, s54
	s_addc_u32 s21, s45, s55
	s_add_u32 s54, s46, s54
	s_addc_u32 s55, s47, s55
	s_lshl_b64 s[56:57], s[50:51], 20
	s_add_u32 s56, s13, s56
	s_addc_u32 s57, s16, s57
	s_and_b32 s30, s60, 0x3c0
	s_ashr_i32 s65, s36, 4
	s_mov_b64 s[58:59], 0
